# final + FILL_A 4 instead of 5 (fewer conversion grabs beside phase A GEMM, more beside phase D)
# baseline (speedup 1.0000x reference)
.LBB0_181:
	s_mul_i32 s6, s90, 0xd760
	s_max_i32 s57, s50, s6
	s_sub_i32 s86, s25, s92
	s_and_b64 s[6:7], s[2:3], exec
	s_movk_i32 s4, 0x80
	s_cselect_b32 s6, s4, 0x100
	s_mul_i32 s6, s6, s86
	s_add_i32 s6, s6, s57
	s_min_i32 s50, s6, 0x34920
	s_cmp_lt_i32 s89, 0
	s_mov_b64 s[6:7], -1
	s_cbranch_scc0 .LBB0_712
	s_andn2_b64 vcc, exec, s[2:3]
	s_not_b32 s68, s89
	s_cbranch_vccnz .LBB0_260
	s_add_u32 s26, s52, 0x37200000
	s_addc_u32 s27, s53, 0
	s_add_u32 s28, s52, 0x5200000
	s_addc_u32 s29, s53, 0
	s_waitcnt vmcnt(0)
	v_mov_b32_e32 v1, v0
	s_cmp_gt_u32 s89, 0xffffffdf
	s_cselect_b64 s[6:7], -1, 0
	s_cmp_lt_u32 s89, 0xffffffe0
	v_readfirstlane_b32 s3, v1
	s_cbranch_scc1 .LBB0_185
	s_lshr_b32 s8, s68, 3
	s_and_b32 s2, s68, 7
	s_lshl_b32 s9, s8, 20
	s_add_u32 s18, s26, s9
	s_addc_u32 s19, s27, 0
	s_lshl_b32 s9, s2, 20
	s_add_u32 s20, s28, s9
	s_addc_u32 s21, s29, 0
	s_lshl_b32 s30, s8, 8
	s_lshl_b32 s2, s2, 8
